# conv1 epilogue staged through LDS, 3 dwordx4 stores per lane instead of 24 short stores
# baseline (speedup 1.0000x reference)
_Z12conv1_kernelPKfS0_S0_PDF16_:
	s_load_dwordx8 s[52:59], s[0:1], 0x0
	v_mul_u32_u24_e32 v1, 49, v0
	v_lshlrev_b32_e32 v10, 2, v0
	v_lshlrev_b32_e32 v58, 2, v1
	s_mul_hi_u32 s0, s2, 0xaaaaaaab
	s_waitcnt lgkmcnt(0)
	global_load_dword v1, v10, s[56:57]
	global_load_dwordx4 v[6:9], v58, s[54:55]
	global_load_dwordx4 v[2:5], v58, s[54:55] offset:16
	global_load_dwordx4 v[26:29], v58, s[54:55] offset:48
	global_load_dwordx4 v[30:33], v58, s[54:55] offset:32
	s_lshr_b32 s33, s0, 4
	s_mov_b32 s1, 0
	s_mul_i32 s4, s33, 24
	s_mul_i32 s0, s33, 0x384
	s_mov_b32 s3, s1
	s_sub_i32 s56, s2, s4
	s_lshl_b64 s[0:1], s[0:1], 2
	s_mul_i32 s2, s56, 30
	s_add_u32 s4, s52, s0
	s_addc_u32 s5, s53, s1
	s_lshl_b64 s[0:1], s[2:3], 2
	s_add_u32 s34, s4, s0
	s_addc_u32 s35, s5, s1
	s_load_dwordx16 s[8:23], s[34:35], 0x0
	global_load_dwordx4 v[10:13], v58, s[54:55] offset:112
	global_load_dwordx4 v[14:17], v58, s[54:55] offset:96
	global_load_dwordx4 v[18:21], v58, s[54:55] offset:80
	global_load_dwordx4 v[22:25], v58, s[54:55] offset:64
	s_load_dwordx16 s[36:51], s[34:35], 0x80
	s_mul_i32 s56, s56, 24
	s_waitcnt vmcnt(7) lgkmcnt(0)
	v_fma_f32 v37, s8, v6, v1
	v_fma_f32 v34, s9, v6, v1
	v_fma_f32 v35, s10, v6, v1
	v_fma_f32 v36, s11, v6, v1
	v_fma_f32 v38, s12, v6, v1
	v_fma_f32 v39, s13, v6, v1
	v_fma_f32 v40, s14, v6, v1
	v_fmac_f32_e32 v37, s9, v7
	v_fmac_f32_e32 v34, s10, v7
	v_fmac_f32_e32 v35, s11, v7
	v_fmac_f32_e32 v36, s12, v7
	v_fmac_f32_e32 v38, s13, v7
	v_fmac_f32_e32 v39, s14, v7
	v_fma_f32 v41, s15, v6, v1
	v_fmac_f32_e32 v40, s15, v7
	v_fmac_f32_e32 v37, s10, v8
	v_fmac_f32_e32 v34, s11, v8
	v_fmac_f32_e32 v35, s12, v8
	v_fmac_f32_e32 v36, s13, v8
	v_fmac_f32_e32 v38, s14, v8
	v_fmac_f32_e32 v39, s15, v8
	v_fma_f32 v42, s16, v6, v1
	v_fmac_f32_e32 v41, s16, v7
	v_fmac_f32_e32 v40, s16, v8
	v_fmac_f32_e32 v37, s11, v9
	v_fmac_f32_e32 v34, s12, v9
	v_fmac_f32_e32 v35, s13, v9
	v_fmac_f32_e32 v36, s14, v9
	v_fmac_f32_e32 v38, s15, v9
	v_fmac_f32_e32 v39, s16, v9
	v_fma_f32 v43, s17, v6, v1
	v_fmac_f32_e32 v42, s17, v7
	v_fmac_f32_e32 v41, s17, v8
	v_fmac_f32_e32 v40, s17, v9
	s_waitcnt vmcnt(6)
	v_fmac_f32_e32 v37, s12, v2
	v_fmac_f32_e32 v34, s13, v2
	v_fmac_f32_e32 v35, s14, v2
	v_fmac_f32_e32 v36, s15, v2
	v_fmac_f32_e32 v38, s16, v2
	v_fmac_f32_e32 v39, s17, v2
	v_fma_f32 v44, s18, v6, v1
	v_fmac_f32_e32 v43, s18, v7
	v_fmac_f32_e32 v42, s18, v8
	v_fmac_f32_e32 v41, s18, v9
	v_fmac_f32_e32 v40, s18, v2
	v_fmac_f32_e32 v37, s13, v3
	v_fmac_f32_e32 v34, s14, v3
	v_fmac_f32_e32 v35, s15, v3
	v_fmac_f32_e32 v36, s16, v3
	v_fmac_f32_e32 v38, s17, v3
	v_fmac_f32_e32 v39, s18, v3
	v_fma_f32 v45, s19, v6, v1
	v_fmac_f32_e32 v44, s19, v7
	v_fmac_f32_e32 v43, s19, v8
	v_fmac_f32_e32 v42, s19, v9
	v_fmac_f32_e32 v41, s19, v2
	v_fmac_f32_e32 v40, s19, v3
	v_fmac_f32_e32 v37, s14, v4
	v_fmac_f32_e32 v34, s15, v4
	v_fmac_f32_e32 v35, s16, v4
	v_fmac_f32_e32 v36, s17, v4
	v_fmac_f32_e32 v38, s18, v4
	v_fmac_f32_e32 v39, s19, v4
	s_load_dwordx16 s[4:19], s[34:35], 0x40
	v_fma_f32 v46, s20, v6, v1
	v_fma_f32 v47, s21, v6, v1
	v_fma_f32 v48, s22, v6, v1
	v_fma_f32 v49, s23, v6, v1
	s_waitcnt lgkmcnt(0)
	v_fma_f32 v50, s4, v6, v1
	v_fma_f32 v51, s5, v6, v1
	v_fma_f32 v52, s6, v6, v1
	v_fma_f32 v53, s7, v6, v1
	v_fma_f32 v54, s8, v6, v1
	v_fma_f32 v55, s9, v6, v1
	v_fmac_f32_e32 v45, s20, v7
	v_fmac_f32_e32 v46, s21, v7
	v_fmac_f32_e32 v47, s22, v7
	v_fmac_f32_e32 v48, s23, v7
	v_fmac_f32_e32 v49, s4, v7
	v_fmac_f32_e32 v50, s5, v7
	v_fmac_f32_e32 v51, s6, v7
	v_fmac_f32_e32 v52, s7, v7
	v_fmac_f32_e32 v53, s8, v7
	v_fmac_f32_e32 v54, s9, v7
	v_fma_f32 v56, s10, v6, v1
	v_fmac_f32_e32 v55, s10, v7
	v_fmac_f32_e32 v44, s20, v8
	v_fmac_f32_e32 v45, s21, v8
	v_fmac_f32_e32 v46, s22, v8
	v_fmac_f32_e32 v47, s23, v8
	v_fmac_f32_e32 v48, s4, v8
	v_fmac_f32_e32 v49, s5, v8
	v_fmac_f32_e32 v50, s6, v8
	v_fmac_f32_e32 v51, s7, v8
	v_fmac_f32_e32 v52, s8, v8
	v_fmac_f32_e32 v53, s9, v8
	v_fmac_f32_e32 v54, s10, v8
	v_fmac_f32_e32 v1, s11, v6
	v_fmac_f32_e32 v56, s11, v7
	v_fmac_f32_e32 v55, s11, v8
	v_fmac_f32_e32 v43, s20, v9
	v_fmac_f32_e32 v44, s21, v9
	v_fmac_f32_e32 v45, s22, v9
	v_fmac_f32_e32 v46, s23, v9
	v_fmac_f32_e32 v47, s4, v9
	v_fmac_f32_e32 v48, s5, v9
	v_fmac_f32_e32 v49, s6, v9
	v_fmac_f32_e32 v50, s7, v9
	v_fmac_f32_e32 v51, s8, v9
	v_fmac_f32_e32 v52, s9, v9
	v_fmac_f32_e32 v53, s10, v9
	v_fmac_f32_e32 v54, s11, v9
	v_fmac_f32_e32 v1, s12, v7
	v_fmac_f32_e32 v56, s12, v8
	v_fmac_f32_e32 v55, s12, v9
	v_fmac_f32_e32 v42, s20, v2
	v_fmac_f32_e32 v43, s21, v2
	v_fmac_f32_e32 v44, s22, v2
	v_fmac_f32_e32 v45, s23, v2
	v_fmac_f32_e32 v46, s4, v2
	v_fmac_f32_e32 v47, s5, v2
	v_fmac_f32_e32 v48, s6, v2
	v_fmac_f32_e32 v49, s7, v2
	v_fmac_f32_e32 v50, s8, v2
	v_fmac_f32_e32 v51, s9, v2
	v_fmac_f32_e32 v52, s10, v2
	v_fmac_f32_e32 v53, s11, v2
	v_fmac_f32_e32 v54, s12, v2
	v_fmac_f32_e32 v1, s13, v8
	v_fmac_f32_e32 v56, s13, v9
	v_fmac_f32_e32 v55, s13, v2
	v_fmac_f32_e32 v41, s20, v3
	v_fmac_f32_e32 v42, s21, v3
	v_fmac_f32_e32 v43, s22, v3
	v_fmac_f32_e32 v44, s23, v3
	v_fmac_f32_e32 v45, s4, v3
	v_fmac_f32_e32 v46, s5, v3
	v_fmac_f32_e32 v47, s6, v3
	v_fmac_f32_e32 v48, s7, v3
	v_fmac_f32_e32 v49, s8, v3
	v_fmac_f32_e32 v50, s9, v3
	v_fmac_f32_e32 v51, s10, v3
	v_fmac_f32_e32 v52, s11, v3
	v_fmac_f32_e32 v53, s12, v3
	v_fmac_f32_e32 v54, s13, v3
	v_fmac_f32_e32 v1, s14, v9
	v_fmac_f32_e32 v56, s14, v2
	v_fmac_f32_e32 v55, s14, v3
	v_fmac_f32_e32 v40, s20, v4
	v_fmac_f32_e32 v41, s21, v4
	v_fmac_f32_e32 v42, s22, v4
	v_fmac_f32_e32 v43, s23, v4
	v_fmac_f32_e32 v44, s4, v4
	v_fmac_f32_e32 v45, s5, v4
	v_fmac_f32_e32 v46, s6, v4
	v_fmac_f32_e32 v47, s7, v4
	v_fmac_f32_e32 v48, s8, v4
	v_fmac_f32_e32 v49, s9, v4
	v_fmac_f32_e32 v50, s10, v4
	v_fmac_f32_e32 v51, s11, v4
	v_fmac_f32_e32 v52, s12, v4
	v_fmac_f32_e32 v53, s13, v4
	v_fmac_f32_e32 v54, s14, v4
	v_fmac_f32_e32 v1, s15, v2
	v_fmac_f32_e32 v56, s15, v3
	v_fmac_f32_e32 v55, s15, v4
	s_load_dwordx16 s[0:15], s[34:35], 0xc0
	v_fmac_f32_e32 v37, s18, v5
	v_fmac_f32_e32 v34, s19, v5
	v_fmac_f32_e32 v35, s36, v5
	v_fmac_f32_e32 v36, s37, v5
	v_fmac_f32_e32 v38, s38, v5
	v_fmac_f32_e32 v39, s39, v5
	v_fmac_f32_e32 v40, s40, v5
	v_fmac_f32_e32 v41, s41, v5
	v_fmac_f32_e32 v42, s42, v5
	v_fmac_f32_e32 v43, s43, v5
	v_fmac_f32_e32 v44, s44, v5
	v_fmac_f32_e32 v45, s45, v5
	v_fmac_f32_e32 v46, s46, v5
	s_waitcnt vmcnt(4)
	v_fmac_f32_e32 v37, s19, v30
	v_fmac_f32_e32 v34, s36, v30
	v_fmac_f32_e32 v35, s37, v30
	v_fmac_f32_e32 v36, s38, v30
	v_fmac_f32_e32 v38, s39, v30
	v_fmac_f32_e32 v39, s40, v30
	v_fmac_f32_e32 v40, s41, v30
	v_fmac_f32_e32 v41, s42, v30
	v_fmac_f32_e32 v42, s43, v30
	v_fmac_f32_e32 v43, s44, v30
	v_fmac_f32_e32 v44, s45, v30
	v_fmac_f32_e32 v45, s46, v30
	v_fmac_f32_e32 v1, s16, v3
	v_fmac_f32_e32 v47, s47, v5
	v_fmac_f32_e32 v37, s36, v31
	v_fmac_f32_e32 v34, s37, v31
	v_fmac_f32_e32 v35, s38, v31
	v_fmac_f32_e32 v36, s39, v31
	v_fmac_f32_e32 v38, s40, v31
	v_fmac_f32_e32 v39, s41, v31
	v_fmac_f32_e32 v40, s42, v31
	v_fmac_f32_e32 v41, s43, v31
	v_fmac_f32_e32 v42, s44, v31
	v_fmac_f32_e32 v43, s45, v31
	v_fmac_f32_e32 v44, s46, v31
	v_fmac_f32_e32 v46, s47, v30
	v_fmac_f32_e32 v45, s47, v31
	v_fmac_f32_e32 v56, s16, v4
	v_fmac_f32_e32 v1, s17, v4
	v_fmac_f32_e32 v48, s48, v5
	v_fmac_f32_e32 v37, s37, v32
	v_fmac_f32_e32 v34, s38, v32
	v_fmac_f32_e32 v35, s39, v32
	v_fmac_f32_e32 v36, s40, v32
	v_fmac_f32_e32 v38, s41, v32
	v_fmac_f32_e32 v39, s42, v32
	v_fmac_f32_e32 v40, s43, v32
	v_fmac_f32_e32 v41, s44, v32
	v_fmac_f32_e32 v42, s45, v32
	v_fmac_f32_e32 v43, s46, v32
	v_fmac_f32_e32 v44, s47, v32
	v_fmac_f32_e32 v47, s48, v30
	v_fmac_f32_e32 v46, s48, v31
	v_fmac_f32_e32 v45, s48, v32
	v_fmac_f32_e32 v49, s49, v5
	v_fmac_f32_e32 v50, s50, v5
	v_fmac_f32_e32 v51, s51, v5
	s_waitcnt lgkmcnt(0)
	v_fmac_f32_e32 v52, s0, v5
	v_fmac_f32_e32 v53, s1, v5
	v_fmac_f32_e32 v54, s2, v5
	v_fmac_f32_e32 v55, s3, v5
	v_fmac_f32_e32 v56, s4, v5
	v_fmac_f32_e32 v1, s5, v5
	v_fmac_f32_e32 v37, s38, v33
	v_fmac_f32_e32 v34, s39, v33
	v_fmac_f32_e32 v35, s40, v33
	v_fmac_f32_e32 v36, s41, v33
	v_fmac_f32_e32 v38, s42, v33
	v_fmac_f32_e32 v39, s43, v33
	v_fmac_f32_e32 v40, s44, v33
	v_fmac_f32_e32 v41, s45, v33
	v_fmac_f32_e32 v42, s46, v33
	v_fmac_f32_e32 v43, s47, v33
	v_fmac_f32_e32 v44, s48, v33
	v_fmac_f32_e32 v48, s49, v30
	v_fmac_f32_e32 v47, s49, v31
	v_fmac_f32_e32 v46, s49, v32
	v_fmac_f32_e32 v45, s49, v33
	v_fmac_f32_e32 v37, s39, v26
	v_fmac_f32_e32 v34, s40, v26
	v_fmac_f32_e32 v35, s41, v26
	v_fmac_f32_e32 v36, s42, v26
	v_fmac_f32_e32 v38, s43, v26
	v_fmac_f32_e32 v39, s44, v26
	v_fmac_f32_e32 v40, s45, v26
	v_fmac_f32_e32 v41, s46, v26
	v_fmac_f32_e32 v42, s47, v26
	v_fmac_f32_e32 v43, s48, v26
	v_fmac_f32_e32 v44, s49, v26
	v_fmac_f32_e32 v49, s50, v30
	v_fmac_f32_e32 v48, s50, v31
	v_fmac_f32_e32 v47, s50, v32
	v_fmac_f32_e32 v46, s50, v33
	v_fmac_f32_e32 v45, s50, v26
	v_fmac_f32_e32 v50, s51, v30
	v_fmac_f32_e32 v51, s0, v30
	v_fmac_f32_e32 v52, s1, v30
	v_fmac_f32_e32 v53, s2, v30
	v_fmac_f32_e32 v54, s3, v30
	v_fmac_f32_e32 v55, s4, v30
	v_fmac_f32_e32 v56, s5, v30
	v_fmac_f32_e32 v1, s6, v30
	global_load_dwordx4 v[2:5], v58, s[54:55] offset:176
	global_load_dwordx4 v[6:9], v58, s[54:55] offset:160
	v_fmac_f32_e32 v37, s40, v27
	v_fmac_f32_e32 v34, s41, v27
	v_fmac_f32_e32 v35, s42, v27
	v_fmac_f32_e32 v36, s43, v27
	v_fmac_f32_e32 v38, s44, v27
	v_fmac_f32_e32 v39, s45, v27
	v_fmac_f32_e32 v40, s46, v27
	v_fmac_f32_e32 v41, s47, v27
	v_fmac_f32_e32 v42, s48, v27
	v_fmac_f32_e32 v43, s49, v27
	v_fmac_f32_e32 v44, s50, v27
	v_fmac_f32_e32 v49, s51, v31
	v_fmac_f32_e32 v48, s51, v32
	v_fmac_f32_e32 v47, s51, v33
	v_fmac_f32_e32 v46, s51, v26
	v_fmac_f32_e32 v45, s51, v27
	v_fmac_f32_e32 v50, s0, v31
	v_fmac_f32_e32 v51, s1, v31
	v_fmac_f32_e32 v52, s2, v31
	v_fmac_f32_e32 v53, s3, v31
	v_fmac_f32_e32 v54, s4, v31
	v_fmac_f32_e32 v55, s5, v31
	v_fmac_f32_e32 v56, s6, v31
	v_fmac_f32_e32 v1, s7, v31
	s_load_dwordx16 s[16:31], s[34:35], 0x100
	s_load_dwordx16 s[36:51], s[34:35], 0x140
	v_fmac_f32_e32 v49, s0, v32
	v_fmac_f32_e32 v50, s1, v32
	v_fmac_f32_e32 v51, s2, v32
	v_fmac_f32_e32 v52, s3, v32
	v_fmac_f32_e32 v53, s4, v32
	v_fmac_f32_e32 v54, s5, v32
	v_fmac_f32_e32 v55, s6, v32
	v_fmac_f32_e32 v56, s7, v32
	v_fmac_f32_e32 v1, s8, v32
	v_fmac_f32_e32 v48, s0, v33
	v_fmac_f32_e32 v49, s1, v33
	v_fmac_f32_e32 v50, s2, v33
	v_fmac_f32_e32 v51, s3, v33
	v_fmac_f32_e32 v52, s4, v33
	v_fmac_f32_e32 v53, s5, v33
	v_fmac_f32_e32 v54, s6, v33
	v_fmac_f32_e32 v55, s7, v33
	v_fmac_f32_e32 v56, s8, v33
	v_fmac_f32_e32 v1, s9, v33
	v_fmac_f32_e32 v47, s0, v26
	v_fmac_f32_e32 v48, s1, v26
	v_fmac_f32_e32 v49, s2, v26
	v_fmac_f32_e32 v50, s3, v26
	v_fmac_f32_e32 v51, s4, v26
	v_fmac_f32_e32 v52, s5, v26
	v_fmac_f32_e32 v53, s6, v26
	v_fmac_f32_e32 v54, s7, v26
	v_fmac_f32_e32 v55, s8, v26
	v_fmac_f32_e32 v56, s9, v26
	v_fmac_f32_e32 v1, s10, v26
	v_fmac_f32_e32 v46, s0, v27
	v_fmac_f32_e32 v47, s1, v27
	v_fmac_f32_e32 v48, s2, v27
	v_fmac_f32_e32 v49, s3, v27
	v_fmac_f32_e32 v50, s4, v27
	v_fmac_f32_e32 v51, s5, v27
	v_fmac_f32_e32 v52, s6, v27
	v_fmac_f32_e32 v53, s7, v27
	v_fmac_f32_e32 v54, s8, v27
	v_fmac_f32_e32 v55, s9, v27
	v_fmac_f32_e32 v56, s10, v27
	v_fmac_f32_e32 v1, s11, v27
	v_fmac_f32_e32 v37, s12, v28
	v_fmac_f32_e32 v34, s13, v28
	v_fmac_f32_e32 v35, s14, v28
	v_fmac_f32_e32 v36, s15, v28
	s_waitcnt lgkmcnt(0)
	v_fmac_f32_e32 v38, s16, v28
	v_fmac_f32_e32 v39, s17, v28
	v_fmac_f32_e32 v40, s18, v28
	v_fmac_f32_e32 v41, s19, v28
	v_fmac_f32_e32 v42, s20, v28
	v_fmac_f32_e32 v43, s21, v28
	v_fmac_f32_e32 v44, s22, v28
	v_fmac_f32_e32 v45, s23, v28
	v_fmac_f32_e32 v46, s24, v28
	v_fmac_f32_e32 v47, s25, v28
	v_fmac_f32_e32 v48, s26, v28
	v_fmac_f32_e32 v49, s27, v28
	v_fmac_f32_e32 v50, s28, v28
	v_fmac_f32_e32 v51, s29, v28
	v_fmac_f32_e32 v52, s30, v28
	v_fmac_f32_e32 v53, s31, v28
	v_fmac_f32_e32 v54, s36, v28
	v_fmac_f32_e32 v55, s37, v28
	v_fmac_f32_e32 v56, s38, v28
	v_fmac_f32_e32 v1, s39, v28
	v_fmac_f32_e32 v37, s13, v29
	v_fmac_f32_e32 v34, s14, v29
	v_fmac_f32_e32 v35, s15, v29
	v_fmac_f32_e32 v36, s16, v29
	v_fmac_f32_e32 v38, s17, v29
	v_fmac_f32_e32 v39, s18, v29
	v_fmac_f32_e32 v40, s19, v29
	v_fmac_f32_e32 v41, s20, v29
	v_fmac_f32_e32 v42, s21, v29
	v_fmac_f32_e32 v43, s22, v29
	v_fmac_f32_e32 v44, s23, v29
	v_fmac_f32_e32 v45, s24, v29
	v_fmac_f32_e32 v46, s25, v29
	v_fmac_f32_e32 v47, s26, v29
	v_fmac_f32_e32 v48, s27, v29
	v_fmac_f32_e32 v49, s28, v29
	v_fmac_f32_e32 v50, s29, v29
	v_fmac_f32_e32 v51, s30, v29
	v_fmac_f32_e32 v52, s31, v29
	v_fmac_f32_e32 v53, s36, v29
	v_fmac_f32_e32 v54, s37, v29
	v_fmac_f32_e32 v55, s38, v29
	v_fmac_f32_e32 v56, s39, v29
	v_fmac_f32_e32 v1, s40, v29
	global_load_dwordx4 v[26:29], v58, s[54:55] offset:144
	global_load_dwordx4 v[30:33], v58, s[54:55] offset:128
	global_load_dword v57, v58, s[54:55] offset:192
	s_waitcnt vmcnt(5)
	v_fmac_f32_e32 v37, s14, v22
	v_fmac_f32_e32 v34, s15, v22
	v_fmac_f32_e32 v37, s15, v23
	v_fmac_f32_e32 v35, s16, v22
	v_fmac_f32_e32 v34, s16, v23
	v_fmac_f32_e32 v36, s17, v22
	v_fmac_f32_e32 v38, s18, v22
	v_fmac_f32_e32 v39, s19, v22
	v_fmac_f32_e32 v40, s20, v22
	v_fmac_f32_e32 v41, s21, v22
	v_fmac_f32_e32 v42, s22, v22
	v_fmac_f32_e32 v43, s23, v22
	v_fmac_f32_e32 v44, s24, v22
	v_fmac_f32_e32 v45, s25, v22
	v_fmac_f32_e32 v46, s26, v22
	v_fmac_f32_e32 v47, s27, v22
	v_fmac_f32_e32 v48, s28, v22
	v_fmac_f32_e32 v49, s29, v22
	s_load_dwordx16 s[0:15], s[34:35], 0x180
	v_fmac_f32_e32 v37, s16, v24
	v_fmac_f32_e32 v35, s17, v23
	v_fmac_f32_e32 v34, s17, v24
	v_fmac_f32_e32 v36, s18, v23
	v_fmac_f32_e32 v38, s19, v23
	v_fmac_f32_e32 v39, s20, v23
	v_fmac_f32_e32 v40, s21, v23
	v_fmac_f32_e32 v41, s22, v23
	v_fmac_f32_e32 v42, s23, v23
	v_fmac_f32_e32 v43, s24, v23
	v_fmac_f32_e32 v44, s25, v23
	v_fmac_f32_e32 v45, s26, v23
	v_fmac_f32_e32 v46, s27, v23
	v_fmac_f32_e32 v47, s28, v23
	v_fmac_f32_e32 v48, s29, v23
	v_fmac_f32_e32 v50, s30, v22
	v_fmac_f32_e32 v49, s30, v23
	v_fmac_f32_e32 v37, s17, v25
	v_fmac_f32_e32 v35, s18, v24
	v_fmac_f32_e32 v34, s18, v25
	v_fmac_f32_e32 v36, s19, v24
	v_fmac_f32_e32 v38, s20, v24
	v_fmac_f32_e32 v39, s21, v24
	v_fmac_f32_e32 v40, s22, v24
	v_fmac_f32_e32 v41, s23, v24
	v_fmac_f32_e32 v42, s24, v24
	v_fmac_f32_e32 v43, s25, v24
	v_fmac_f32_e32 v44, s26, v24
	v_fmac_f32_e32 v45, s27, v24
	v_fmac_f32_e32 v46, s28, v24
	v_fmac_f32_e32 v47, s29, v24
	v_fmac_f32_e32 v48, s30, v24
	v_fmac_f32_e32 v51, s31, v22
	v_fmac_f32_e32 v50, s31, v23
	v_fmac_f32_e32 v49, s31, v24
	v_fmac_f32_e32 v37, s18, v18
	v_fmac_f32_e32 v35, s19, v25
	v_fmac_f32_e32 v34, s19, v18
	v_fmac_f32_e32 v36, s20, v25
	v_fmac_f32_e32 v38, s21, v25
	v_fmac_f32_e32 v39, s22, v25
	v_fmac_f32_e32 v40, s23, v25
	v_fmac_f32_e32 v41, s24, v25
	v_fmac_f32_e32 v42, s25, v25
	v_fmac_f32_e32 v43, s26, v25
	v_fmac_f32_e32 v44, s27, v25
	v_fmac_f32_e32 v45, s28, v25
	v_fmac_f32_e32 v46, s29, v25
	v_fmac_f32_e32 v47, s30, v25
	v_fmac_f32_e32 v48, s31, v25
	v_fmac_f32_e32 v52, s36, v22
	v_fmac_f32_e32 v51, s36, v23
	v_fmac_f32_e32 v50, s36, v24
	v_fmac_f32_e32 v49, s36, v25
	v_fmac_f32_e32 v35, s20, v18
	v_fmac_f32_e32 v36, s21, v18
	v_fmac_f32_e32 v38, s22, v18
	v_fmac_f32_e32 v39, s23, v18
	v_fmac_f32_e32 v40, s24, v18
	v_fmac_f32_e32 v41, s25, v18
	v_fmac_f32_e32 v42, s26, v18
	v_fmac_f32_e32 v43, s27, v18
	v_fmac_f32_e32 v44, s28, v18
	v_fmac_f32_e32 v45, s29, v18
	v_fmac_f32_e32 v46, s30, v18
	v_fmac_f32_e32 v47, s31, v18
	v_fmac_f32_e32 v48, s36, v18
	v_fmac_f32_e32 v53, s37, v22
	v_fmac_f32_e32 v52, s37, v23
	v_fmac_f32_e32 v51, s37, v24
	v_fmac_f32_e32 v50, s37, v25
	v_fmac_f32_e32 v49, s37, v18
	v_fmac_f32_e32 v37, s46, v19
	v_fmac_f32_e32 v34, s47, v19
	v_fmac_f32_e32 v54, s38, v22
	v_fmac_f32_e32 v53, s38, v23
	v_fmac_f32_e32 v52, s38, v24
	v_fmac_f32_e32 v51, s38, v25
	v_fmac_f32_e32 v50, s38, v18
	v_fmac_f32_e32 v37, s47, v20
	v_fmac_f32_e32 v35, s48, v19
	v_fmac_f32_e32 v34, s48, v20
	v_fmac_f32_e32 v36, s49, v19
	v_fmac_f32_e32 v38, s50, v19
	v_fmac_f32_e32 v39, s51, v19
	s_waitcnt lgkmcnt(0)
	v_fmac_f32_e32 v40, s0, v19
	v_fmac_f32_e32 v41, s1, v19
	v_fmac_f32_e32 v42, s2, v19
	v_fmac_f32_e32 v43, s3, v19
	v_fmac_f32_e32 v44, s4, v19
	v_fmac_f32_e32 v45, s5, v19
	v_fmac_f32_e32 v46, s6, v19
	v_fmac_f32_e32 v47, s7, v19
	v_fmac_f32_e32 v48, s8, v19
	v_fmac_f32_e32 v49, s9, v19
	v_fmac_f32_e32 v55, s39, v22
	v_fmac_f32_e32 v54, s39, v23
	v_fmac_f32_e32 v53, s39, v24
	v_fmac_f32_e32 v52, s39, v25
	v_fmac_f32_e32 v51, s39, v18
	v_fmac_f32_e32 v56, s40, v22
	v_fmac_f32_e32 v1, s41, v22
	v_fmac_f32_e32 v37, s48, v21
	v_fmac_f32_e32 v35, s49, v20
	v_fmac_f32_e32 v34, s49, v21
	v_fmac_f32_e32 v36, s50, v20
	v_fmac_f32_e32 v38, s51, v20
	v_fmac_f32_e32 v39, s0, v20
	v_fmac_f32_e32 v40, s1, v20
	v_fmac_f32_e32 v41, s2, v20
	v_fmac_f32_e32 v42, s3, v20
	v_fmac_f32_e32 v43, s4, v20
	v_fmac_f32_e32 v44, s5, v20
	v_fmac_f32_e32 v45, s6, v20
	v_fmac_f32_e32 v46, s7, v20
	v_fmac_f32_e32 v47, s8, v20
	v_fmac_f32_e32 v48, s9, v20
	v_fmac_f32_e32 v50, s10, v19
	v_fmac_f32_e32 v49, s10, v20
	s_load_dwordx16 s[16:31], s[34:35], 0x1c0
	v_fmac_f32_e32 v55, s40, v23
	v_fmac_f32_e32 v54, s40, v24
	v_fmac_f32_e32 v53, s40, v25
	v_fmac_f32_e32 v52, s40, v18
	v_fmac_f32_e32 v56, s41, v23
	v_fmac_f32_e32 v1, s42, v23
	v_fmac_f32_e32 v37, s49, v14
	v_fmac_f32_e32 v35, s50, v21
	v_fmac_f32_e32 v34, s50, v14
	v_fmac_f32_e32 v36, s51, v21
	v_fmac_f32_e32 v38, s0, v21
	v_fmac_f32_e32 v39, s1, v21
	v_fmac_f32_e32 v40, s2, v21
	v_fmac_f32_e32 v41, s3, v21
	v_fmac_f32_e32 v42, s4, v21
	v_fmac_f32_e32 v43, s5, v21
	v_fmac_f32_e32 v44, s6, v21
	v_fmac_f32_e32 v45, s7, v21
	v_fmac_f32_e32 v46, s8, v21
	v_fmac_f32_e32 v47, s9, v21
	v_fmac_f32_e32 v48, s10, v21
	v_fmac_f32_e32 v51, s11, v19
	v_fmac_f32_e32 v50, s11, v20
	v_fmac_f32_e32 v49, s11, v21
	v_fmac_f32_e32 v55, s41, v24
	v_fmac_f32_e32 v54, s41, v25
	v_fmac_f32_e32 v53, s41, v18
	v_fmac_f32_e32 v56, s42, v24
	v_fmac_f32_e32 v1, s43, v24
	v_fmac_f32_e32 v37, s50, v15
	v_fmac_f32_e32 v35, s51, v14
	v_fmac_f32_e32 v34, s51, v15
	v_fmac_f32_e32 v36, s0, v14
	v_fmac_f32_e32 v38, s1, v14
	v_fmac_f32_e32 v39, s2, v14
	v_fmac_f32_e32 v40, s3, v14
	v_fmac_f32_e32 v41, s4, v14
	v_fmac_f32_e32 v42, s5, v14
	v_fmac_f32_e32 v43, s6, v14
	v_fmac_f32_e32 v44, s7, v14
	v_fmac_f32_e32 v45, s8, v14
	v_fmac_f32_e32 v46, s9, v14
	v_fmac_f32_e32 v47, s10, v14
	v_fmac_f32_e32 v48, s11, v14
	v_fmac_f32_e32 v52, s12, v19
	v_fmac_f32_e32 v51, s12, v20
	v_fmac_f32_e32 v50, s12, v21
	v_fmac_f32_e32 v49, s12, v14
	v_fmac_f32_e32 v55, s42, v25
	v_fmac_f32_e32 v54, s42, v18
	v_fmac_f32_e32 v56, s43, v25
	v_fmac_f32_e32 v1, s44, v25
	v_fmac_f32_e32 v37, s51, v16
	v_fmac_f32_e32 v35, s0, v15
	v_fmac_f32_e32 v34, s0, v16
	v_fmac_f32_e32 v36, s1, v15
	v_fmac_f32_e32 v38, s2, v15
	v_fmac_f32_e32 v39, s3, v15
	v_fmac_f32_e32 v40, s4, v15
	v_fmac_f32_e32 v41, s5, v15
	v_fmac_f32_e32 v42, s6, v15
	v_fmac_f32_e32 v43, s7, v15
	v_fmac_f32_e32 v44, s8, v15
	v_fmac_f32_e32 v45, s9, v15
	v_fmac_f32_e32 v46, s10, v15
	v_fmac_f32_e32 v47, s11, v15
	v_fmac_f32_e32 v48, s12, v15
	v_fmac_f32_e32 v53, s13, v19
	v_fmac_f32_e32 v52, s13, v20
	v_fmac_f32_e32 v51, s13, v21
	v_fmac_f32_e32 v50, s13, v14
	v_fmac_f32_e32 v49, s13, v15
	v_fmac_f32_e32 v55, s43, v18
	v_fmac_f32_e32 v56, s44, v18
	v_fmac_f32_e32 v1, s45, v18
	v_fmac_f32_e32 v37, s0, v17
	v_fmac_f32_e32 v35, s1, v16
	v_fmac_f32_e32 v34, s1, v17
	v_fmac_f32_e32 v36, s2, v16
	v_fmac_f32_e32 v38, s3, v16
	v_fmac_f32_e32 v39, s4, v16
	v_fmac_f32_e32 v40, s5, v16
	v_fmac_f32_e32 v41, s6, v16
	v_fmac_f32_e32 v42, s7, v16
	v_fmac_f32_e32 v43, s8, v16
	v_fmac_f32_e32 v44, s9, v16
	v_fmac_f32_e32 v45, s10, v16
	v_fmac_f32_e32 v46, s11, v16
	v_fmac_f32_e32 v47, s12, v16
	v_fmac_f32_e32 v48, s13, v16
	v_fmac_f32_e32 v54, s14, v19
	v_fmac_f32_e32 v53, s14, v20
	v_fmac_f32_e32 v52, s14, v21
	v_fmac_f32_e32 v51, s14, v14
	v_fmac_f32_e32 v50, s14, v15
	v_fmac_f32_e32 v49, s14, v16
	v_fmac_f32_e32 v35, s2, v17
	v_fmac_f32_e32 v36, s3, v17
	v_fmac_f32_e32 v38, s4, v17
	v_fmac_f32_e32 v39, s5, v17
	v_fmac_f32_e32 v40, s6, v17
	v_fmac_f32_e32 v41, s7, v17
	v_fmac_f32_e32 v42, s8, v17
	v_fmac_f32_e32 v43, s9, v17
	v_fmac_f32_e32 v44, s10, v17
	v_fmac_f32_e32 v45, s11, v17
	v_fmac_f32_e32 v46, s12, v17
	v_fmac_f32_e32 v47, s13, v17
	v_fmac_f32_e32 v48, s14, v17
	v_fmac_f32_e32 v55, s15, v19
	v_fmac_f32_e32 v54, s15, v20
	v_fmac_f32_e32 v53, s15, v21
	v_fmac_f32_e32 v52, s15, v14
	v_fmac_f32_e32 v51, s15, v15
	v_fmac_f32_e32 v50, s15, v16
	v_fmac_f32_e32 v49, s15, v17
	s_waitcnt lgkmcnt(0)
	v_fmac_f32_e32 v56, s16, v19
	v_fmac_f32_e32 v1, s17, v19
	v_fmac_f32_e32 v37, s24, v10
	v_fmac_f32_e32 v34, s25, v10
	s_load_dwordx16 s[0:15], s[34:35], 0x200
	v_fmac_f32_e32 v55, s16, v20
	v_fmac_f32_e32 v56, s17, v20
	v_fmac_f32_e32 v1, s18, v20
	v_fmac_f32_e32 v37, s25, v11
	v_fmac_f32_e32 v35, s26, v10
	v_fmac_f32_e32 v34, s26, v11
	v_fmac_f32_e32 v54, s16, v21
	v_fmac_f32_e32 v55, s17, v21
	v_fmac_f32_e32 v56, s18, v21
	v_fmac_f32_e32 v1, s19, v21
	v_fmac_f32_e32 v37, s26, v12
	v_fmac_f32_e32 v36, s27, v10
	v_fmac_f32_e32 v35, s27, v11
	v_fmac_f32_e32 v34, s27, v12
	v_fmac_f32_e32 v53, s16, v14
	v_fmac_f32_e32 v52, s16, v15
	v_fmac_f32_e32 v51, s16, v16
	v_fmac_f32_e32 v54, s17, v14
	v_fmac_f32_e32 v55, s18, v14
	v_fmac_f32_e32 v56, s19, v14
	v_fmac_f32_e32 v1, s20, v14
	v_fmac_f32_e32 v37, s27, v13
	v_fmac_f32_e32 v38, s28, v10
	v_fmac_f32_e32 v36, s28, v11
	v_fmac_f32_e32 v35, s28, v12
	v_fmac_f32_e32 v34, s28, v13
	v_fmac_f32_e32 v50, s16, v17
	v_fmac_f32_e32 v53, s17, v15
	v_fmac_f32_e32 v52, s17, v16
	v_fmac_f32_e32 v51, s17, v17
	v_fmac_f32_e32 v54, s18, v15
	v_fmac_f32_e32 v55, s19, v15
	v_fmac_f32_e32 v56, s20, v15
	v_fmac_f32_e32 v1, s21, v15
	s_waitcnt vmcnt(1)
	v_fmac_f32_e32 v37, s28, v30
	v_fmac_f32_e32 v39, s29, v10
	v_fmac_f32_e32 v38, s29, v11
	v_fmac_f32_e32 v36, s29, v12
	v_fmac_f32_e32 v35, s29, v13
	v_fmac_f32_e32 v34, s29, v30
	v_fmac_f32_e32 v53, s18, v16
	v_fmac_f32_e32 v52, s18, v17
	v_fmac_f32_e32 v54, s19, v16
	v_fmac_f32_e32 v55, s20, v16
	v_fmac_f32_e32 v56, s21, v16
	v_fmac_f32_e32 v1, s22, v16
	v_fmac_f32_e32 v37, s29, v31
	v_fmac_f32_e32 v40, s30, v10
	v_fmac_f32_e32 v39, s30, v11
	v_fmac_f32_e32 v38, s30, v12
	v_fmac_f32_e32 v36, s30, v13
	v_fmac_f32_e32 v35, s30, v30
	v_fmac_f32_e32 v34, s30, v31
	v_fmac_f32_e32 v41, s31, v10
	s_waitcnt lgkmcnt(0)
	v_fmac_f32_e32 v42, s0, v10
	v_fmac_f32_e32 v43, s1, v10
	v_fmac_f32_e32 v44, s2, v10
	v_fmac_f32_e32 v45, s3, v10
	v_fmac_f32_e32 v46, s4, v10
	v_fmac_f32_e32 v47, s5, v10
	v_fmac_f32_e32 v48, s6, v10
	v_fmac_f32_e32 v49, s7, v10
	v_fmac_f32_e32 v50, s8, v10
	v_fmac_f32_e32 v51, s9, v10
	v_fmac_f32_e32 v53, s19, v17
	v_fmac_f32_e32 v54, s20, v17
	v_fmac_f32_e32 v55, s21, v17
	v_fmac_f32_e32 v56, s22, v17
	v_fmac_f32_e32 v1, s23, v17
	v_fmac_f32_e32 v37, s30, v32
	v_fmac_f32_e32 v40, s31, v11
	v_fmac_f32_e32 v39, s31, v12
	v_fmac_f32_e32 v38, s31, v13
	v_fmac_f32_e32 v36, s31, v30
	v_fmac_f32_e32 v35, s31, v31
	v_fmac_f32_e32 v34, s31, v32
	v_fmac_f32_e32 v41, s0, v11
	v_fmac_f32_e32 v42, s1, v11
	v_fmac_f32_e32 v43, s2, v11
	v_fmac_f32_e32 v44, s3, v11
	v_fmac_f32_e32 v45, s4, v11
	v_fmac_f32_e32 v46, s5, v11
	v_fmac_f32_e32 v47, s6, v11
	v_fmac_f32_e32 v48, s7, v11
	v_fmac_f32_e32 v49, s8, v11
	v_fmac_f32_e32 v50, s9, v11
	v_fmac_f32_e32 v52, s10, v10
	v_fmac_f32_e32 v51, s10, v11
	s_load_dwordx16 s[16:31], s[34:35], 0x240
	v_fmac_f32_e32 v40, s0, v12
	v_fmac_f32_e32 v41, s1, v12
	v_fmac_f32_e32 v42, s2, v12
	v_fmac_f32_e32 v43, s3, v12
	v_fmac_f32_e32 v44, s4, v12
	v_fmac_f32_e32 v45, s5, v12
	v_fmac_f32_e32 v46, s6, v12
	v_fmac_f32_e32 v47, s7, v12
	v_fmac_f32_e32 v48, s8, v12
	v_fmac_f32_e32 v49, s9, v12
	v_fmac_f32_e32 v50, s10, v12
	v_fmac_f32_e32 v53, s11, v10
	v_fmac_f32_e32 v52, s11, v11
	v_fmac_f32_e32 v51, s11, v12
	v_fmac_f32_e32 v39, s0, v13
	v_fmac_f32_e32 v40, s1, v13
	v_fmac_f32_e32 v41, s2, v13
	v_fmac_f32_e32 v42, s3, v13
	v_fmac_f32_e32 v43, s4, v13
	v_fmac_f32_e32 v44, s5, v13
	v_fmac_f32_e32 v45, s6, v13
	v_fmac_f32_e32 v46, s7, v13
	v_fmac_f32_e32 v47, s8, v13
	v_fmac_f32_e32 v48, s9, v13
	v_fmac_f32_e32 v49, s10, v13
	v_fmac_f32_e32 v50, s11, v13
	v_fmac_f32_e32 v54, s12, v10
	v_fmac_f32_e32 v53, s12, v11
	v_fmac_f32_e32 v52, s12, v12
	v_fmac_f32_e32 v51, s12, v13
	v_fmac_f32_e32 v38, s0, v30
	v_fmac_f32_e32 v36, s0, v31
	v_fmac_f32_e32 v39, s1, v30
	v_fmac_f32_e32 v40, s2, v30
	v_fmac_f32_e32 v41, s3, v30
	v_fmac_f32_e32 v42, s4, v30
	v_fmac_f32_e32 v43, s5, v30
	v_fmac_f32_e32 v44, s6, v30
	v_fmac_f32_e32 v45, s7, v30
	v_fmac_f32_e32 v46, s8, v30
	v_fmac_f32_e32 v47, s9, v30
	v_fmac_f32_e32 v48, s10, v30
	v_fmac_f32_e32 v49, s11, v30
	v_fmac_f32_e32 v50, s12, v30
	v_fmac_f32_e32 v55, s13, v10
	v_fmac_f32_e32 v54, s13, v11
	v_fmac_f32_e32 v53, s13, v12
	v_fmac_f32_e32 v52, s13, v13
	v_fmac_f32_e32 v51, s13, v30
	v_fmac_f32_e32 v35, s0, v32
	v_fmac_f32_e32 v38, s1, v31
	v_fmac_f32_e32 v36, s1, v32
	v_fmac_f32_e32 v39, s2, v31
	v_fmac_f32_e32 v40, s3, v31
	v_fmac_f32_e32 v41, s4, v31
	v_fmac_f32_e32 v42, s5, v31
	v_fmac_f32_e32 v43, s6, v31
	v_fmac_f32_e32 v44, s7, v31
	v_fmac_f32_e32 v45, s8, v31
	v_fmac_f32_e32 v46, s9, v31
	v_fmac_f32_e32 v47, s10, v31
	v_fmac_f32_e32 v48, s11, v31
	v_fmac_f32_e32 v49, s12, v31
	v_fmac_f32_e32 v50, s13, v31
	v_fmac_f32_e32 v56, s14, v10
	v_fmac_f32_e32 v55, s14, v11
	v_fmac_f32_e32 v54, s14, v12
	v_fmac_f32_e32 v53, s14, v13
	v_fmac_f32_e32 v52, s14, v30
	v_fmac_f32_e32 v51, s14, v31
	v_fmac_f32_e32 v38, s2, v32
	v_fmac_f32_e32 v39, s3, v32
	v_fmac_f32_e32 v40, s4, v32
	v_fmac_f32_e32 v41, s5, v32
	v_fmac_f32_e32 v42, s6, v32
	v_fmac_f32_e32 v43, s7, v32
	v_fmac_f32_e32 v44, s8, v32
	v_fmac_f32_e32 v45, s9, v32
	v_fmac_f32_e32 v46, s10, v32
	v_fmac_f32_e32 v47, s11, v32
	v_fmac_f32_e32 v48, s12, v32
	v_fmac_f32_e32 v49, s13, v32
	v_fmac_f32_e32 v50, s14, v32
	v_fmac_f32_e32 v1, s15, v10
	v_fmac_f32_e32 v56, s15, v11
	v_fmac_f32_e32 v55, s15, v12
	v_fmac_f32_e32 v54, s15, v13
	v_fmac_f32_e32 v53, s15, v30
	v_fmac_f32_e32 v52, s15, v31
	v_fmac_f32_e32 v51, s15, v32
	s_waitcnt lgkmcnt(0)
	v_fmac_f32_e32 v37, s22, v33
	v_fmac_f32_e32 v34, s23, v33
	v_fmac_f32_e32 v35, s24, v33
	v_fmac_f32_e32 v36, s25, v33
	s_load_dwordx16 s[0:15], s[34:35], 0x280
	v_fmac_f32_e32 v1, s16, v11
	v_fmac_f32_e32 v37, s23, v26
	v_fmac_f32_e32 v34, s24, v26
	v_fmac_f32_e32 v35, s25, v26
	v_fmac_f32_e32 v38, s26, v33
	v_fmac_f32_e32 v36, s26, v26
	v_fmac_f32_e32 v56, s16, v12
	v_fmac_f32_e32 v1, s17, v12
	v_fmac_f32_e32 v37, s24, v27
	v_fmac_f32_e32 v34, s25, v27
	v_fmac_f32_e32 v35, s26, v27
	v_fmac_f32_e32 v39, s27, v33
	v_fmac_f32_e32 v38, s27, v26
	v_fmac_f32_e32 v36, s27, v27
	v_fmac_f32_e32 v55, s16, v13
	v_fmac_f32_e32 v54, s16, v30
	v_fmac_f32_e32 v53, s16, v31
	v_fmac_f32_e32 v56, s17, v13
	v_fmac_f32_e32 v1, s18, v13
	v_fmac_f32_e32 v37, s25, v28
	v_fmac_f32_e32 v34, s26, v28
	v_fmac_f32_e32 v35, s27, v28
	v_fmac_f32_e32 v40, s28, v33
	v_fmac_f32_e32 v39, s28, v26
	v_fmac_f32_e32 v38, s28, v27
	v_fmac_f32_e32 v36, s28, v28
	v_fmac_f32_e32 v52, s16, v32
	v_fmac_f32_e32 v55, s17, v30
	v_fmac_f32_e32 v54, s17, v31
	v_fmac_f32_e32 v53, s17, v32
	v_fmac_f32_e32 v56, s18, v30
	v_fmac_f32_e32 v1, s19, v30
	v_fmac_f32_e32 v37, s26, v29
	v_fmac_f32_e32 v34, s27, v29
	v_fmac_f32_e32 v35, s28, v29
	v_fmac_f32_e32 v41, s29, v33
	v_fmac_f32_e32 v40, s29, v26
	v_fmac_f32_e32 v39, s29, v27
	v_fmac_f32_e32 v38, s29, v28
	v_fmac_f32_e32 v36, s29, v29
	v_fmac_f32_e32 v55, s18, v31
	v_fmac_f32_e32 v54, s18, v32
	v_fmac_f32_e32 v56, s19, v31
	v_fmac_f32_e32 v1, s20, v31
	v_fmac_f32_e32 v37, s27, v6
	v_fmac_f32_e32 v34, s28, v6
	v_fmac_f32_e32 v35, s29, v6
	v_fmac_f32_e32 v42, s30, v33
	v_fmac_f32_e32 v41, s30, v26
	v_fmac_f32_e32 v40, s30, v27
	v_fmac_f32_e32 v39, s30, v28
	v_fmac_f32_e32 v38, s30, v29
	v_fmac_f32_e32 v36, s30, v6
	v_fmac_f32_e32 v43, s31, v33
	s_waitcnt lgkmcnt(0)
	v_fmac_f32_e32 v44, s0, v33
	v_fmac_f32_e32 v45, s1, v33
	v_fmac_f32_e32 v46, s2, v33
	v_fmac_f32_e32 v47, s3, v33
	v_fmac_f32_e32 v48, s4, v33
	v_fmac_f32_e32 v49, s5, v33
	v_fmac_f32_e32 v50, s6, v33
	v_fmac_f32_e32 v51, s7, v33
	v_fmac_f32_e32 v52, s8, v33
	v_fmac_f32_e32 v53, s9, v33
	v_fmac_f32_e32 v55, s19, v32
	v_fmac_f32_e32 v56, s20, v32
	v_fmac_f32_e32 v1, s21, v32
	v_fmac_f32_e32 v37, s28, v7
	v_fmac_f32_e32 v34, s29, v7
	v_fmac_f32_e32 v35, s30, v7
	v_fmac_f32_e32 v42, s31, v26
	v_fmac_f32_e32 v41, s31, v27
	v_fmac_f32_e32 v40, s31, v28
	v_fmac_f32_e32 v39, s31, v29
	v_fmac_f32_e32 v38, s31, v6
	v_fmac_f32_e32 v36, s31, v7
	v_fmac_f32_e32 v43, s0, v26
	v_fmac_f32_e32 v44, s1, v26
	v_fmac_f32_e32 v45, s2, v26
	v_fmac_f32_e32 v46, s3, v26
	v_fmac_f32_e32 v47, s4, v26
	v_fmac_f32_e32 v48, s5, v26
	v_fmac_f32_e32 v49, s6, v26
	v_fmac_f32_e32 v50, s7, v26
	v_fmac_f32_e32 v51, s8, v26
	v_fmac_f32_e32 v52, s9, v26
	v_fmac_f32_e32 v54, s10, v33
	v_fmac_f32_e32 v53, s10, v26
	s_load_dwordx16 s[16:31], s[34:35], 0x2c0
	v_fmac_f32_e32 v42, s0, v27
	v_fmac_f32_e32 v41, s0, v28
	v_fmac_f32_e32 v43, s1, v27
	v_fmac_f32_e32 v44, s2, v27
	v_fmac_f32_e32 v45, s3, v27
	v_fmac_f32_e32 v46, s4, v27
	v_fmac_f32_e32 v47, s5, v27
	v_fmac_f32_e32 v48, s6, v27
	v_fmac_f32_e32 v49, s7, v27
	v_fmac_f32_e32 v50, s8, v27
	v_fmac_f32_e32 v51, s9, v27
	v_fmac_f32_e32 v52, s10, v27
	v_fmac_f32_e32 v55, s11, v33
	v_fmac_f32_e32 v54, s11, v26
	v_fmac_f32_e32 v53, s11, v27
	v_fmac_f32_e32 v40, s0, v29
	v_fmac_f32_e32 v42, s1, v28
	v_fmac_f32_e32 v41, s1, v29
	v_fmac_f32_e32 v43, s2, v28
	v_fmac_f32_e32 v44, s3, v28
	v_fmac_f32_e32 v45, s4, v28
	v_fmac_f32_e32 v46, s5, v28
	v_fmac_f32_e32 v47, s6, v28
	v_fmac_f32_e32 v48, s7, v28
	v_fmac_f32_e32 v49, s8, v28
	v_fmac_f32_e32 v50, s9, v28
	v_fmac_f32_e32 v51, s10, v28
	v_fmac_f32_e32 v52, s11, v28
	v_fmac_f32_e32 v56, s12, v33
	v_fmac_f32_e32 v55, s12, v26
	v_fmac_f32_e32 v54, s12, v27
	v_fmac_f32_e32 v53, s12, v28
	v_fmac_f32_e32 v40, s1, v6
	v_fmac_f32_e32 v42, s2, v29
	v_fmac_f32_e32 v41, s2, v6
	v_fmac_f32_e32 v43, s3, v29
	v_fmac_f32_e32 v44, s4, v29
	v_fmac_f32_e32 v45, s5, v29
	v_fmac_f32_e32 v46, s6, v29
	v_fmac_f32_e32 v47, s7, v29
	v_fmac_f32_e32 v48, s8, v29
	v_fmac_f32_e32 v49, s9, v29
	v_fmac_f32_e32 v50, s10, v29
	v_fmac_f32_e32 v51, s11, v29
	v_fmac_f32_e32 v52, s12, v29
	v_fmac_f32_e32 v1, s13, v33
	v_fmac_f32_e32 v56, s13, v26
	v_fmac_f32_e32 v55, s13, v27
	v_fmac_f32_e32 v54, s13, v28
	v_fmac_f32_e32 v53, s13, v29
	v_fmac_f32_e32 v39, s0, v6
	v_fmac_f32_e32 v40, s2, v7
	v_fmac_f32_e32 v42, s3, v6
	v_fmac_f32_e32 v41, s3, v7
	v_fmac_f32_e32 v43, s4, v6
	v_fmac_f32_e32 v44, s5, v6
	v_fmac_f32_e32 v45, s6, v6
	v_fmac_f32_e32 v46, s7, v6
	v_fmac_f32_e32 v47, s8, v6
	v_fmac_f32_e32 v48, s9, v6
	v_fmac_f32_e32 v49, s10, v6
	v_fmac_f32_e32 v50, s11, v6
	v_fmac_f32_e32 v51, s12, v6
	v_fmac_f32_e32 v52, s13, v6
	v_fmac_f32_e32 v1, s14, v26
	v_fmac_f32_e32 v56, s14, v27
	v_fmac_f32_e32 v55, s14, v28
	v_fmac_f32_e32 v54, s14, v29
	v_fmac_f32_e32 v53, s14, v6
	v_fmac_f32_e32 v38, s0, v7
	v_fmac_f32_e32 v39, s1, v7
	v_fmac_f32_e32 v42, s4, v7
	v_fmac_f32_e32 v43, s5, v7
	v_fmac_f32_e32 v44, s6, v7
	v_fmac_f32_e32 v45, s7, v7
	v_fmac_f32_e32 v46, s8, v7
	v_fmac_f32_e32 v47, s9, v7
	v_fmac_f32_e32 v48, s10, v7
	v_fmac_f32_e32 v49, s11, v7
	v_fmac_f32_e32 v50, s12, v7
	v_fmac_f32_e32 v51, s13, v7
	v_fmac_f32_e32 v52, s14, v7
	v_fmac_f32_e32 v1, s15, v27
	v_fmac_f32_e32 v56, s15, v28
	v_fmac_f32_e32 v55, s15, v29
	v_fmac_f32_e32 v54, s15, v6
	v_fmac_f32_e32 v53, s15, v7
	s_waitcnt lgkmcnt(0)
	v_fmac_f32_e32 v40, s26, v8
	v_fmac_f32_e32 v41, s27, v8
	s_load_dwordx16 s[0:15], s[34:35], 0x300
	v_fmac_f32_e32 v40, s27, v9
	v_fmac_f32_e32 v42, s28, v8
	v_fmac_f32_e32 v41, s28, v9
	v_fmac_f32_e32 v1, s16, v28
	v_fmac_f32_e32 v56, s16, v29
	v_fmac_f32_e32 v40, s28, v2
	v_fmac_f32_e32 v43, s29, v8
	v_fmac_f32_e32 v42, s29, v9
	v_fmac_f32_e32 v41, s29, v2
	v_fmac_f32_e32 v1, s17, v29
	v_fmac_f32_e32 v56, s17, v6
	v_fmac_f32_e32 v40, s29, v3
	v_fmac_f32_e32 v44, s30, v8
	v_fmac_f32_e32 v43, s30, v9
	v_fmac_f32_e32 v42, s30, v2
	v_fmac_f32_e32 v41, s30, v3
	v_fmac_f32_e32 v1, s18, v6
	v_fmac_f32_e32 v56, s18, v7
	v_fmac_f32_e32 v40, s30, v4
	v_fmac_f32_e32 v45, s31, v8
	v_fmac_f32_e32 v44, s31, v9
	v_fmac_f32_e32 v43, s31, v2
	v_fmac_f32_e32 v42, s31, v3
	v_fmac_f32_e32 v41, s31, v4
	v_fmac_f32_e32 v55, s16, v6
	v_fmac_f32_e32 v1, s19, v7
	v_fmac_f32_e32 v40, s31, v5
	s_waitcnt lgkmcnt(0)
	v_fmac_f32_e32 v46, s0, v8
	v_fmac_f32_e32 v45, s0, v9
	v_fmac_f32_e32 v44, s0, v2
	v_fmac_f32_e32 v43, s0, v3
	v_fmac_f32_e32 v42, s0, v4
	v_fmac_f32_e32 v41, s0, v5
	v_fmac_f32_e32 v56, s10, v8
	v_fmac_f32_e32 v54, s16, v7
	v_fmac_f32_e32 v55, s17, v7
	s_waitcnt vmcnt(0)
	v_fmac_f32_e32 v40, s0, v57
	v_fmac_f32_e32 v47, s1, v8
	v_fmac_f32_e32 v46, s1, v9
	v_fmac_f32_e32 v45, s1, v2
	v_fmac_f32_e32 v44, s1, v3
	v_fmac_f32_e32 v43, s1, v4
	v_fmac_f32_e32 v42, s1, v5
	v_fmac_f32_e32 v41, s1, v57
	v_fmac_f32_e32 v1, s11, v8
	v_fmac_f32_e32 v56, s11, v9
	s_load_dwordx2 s[0:1], s[34:35], 0x340
	v_fmac_f32_e32 v37, s20, v8
	v_fmac_f32_e32 v34, s21, v8
	v_fmac_f32_e32 v35, s22, v8
	v_fmac_f32_e32 v36, s23, v8
	v_fmac_f32_e32 v38, s24, v8
	v_fmac_f32_e32 v39, s25, v8
	v_fmac_f32_e32 v48, s2, v8
	v_fmac_f32_e32 v49, s3, v8
	v_fmac_f32_e32 v50, s4, v8
	v_fmac_f32_e32 v51, s5, v8
	v_fmac_f32_e32 v52, s6, v8
	v_fmac_f32_e32 v53, s7, v8
	v_fmac_f32_e32 v54, s8, v8
	v_fmac_f32_e32 v55, s9, v8
	v_fmac_f32_e32 v1, s12, v9
	v_fmac_f32_e32 v56, s12, v2
	v_fmac_f32_e32 v37, s21, v9
	v_fmac_f32_e32 v34, s22, v9
	v_fmac_f32_e32 v35, s23, v9
	v_fmac_f32_e32 v36, s24, v9
	v_fmac_f32_e32 v38, s25, v9
	v_fmac_f32_e32 v39, s26, v9
	v_fmac_f32_e32 v47, s2, v9
	v_fmac_f32_e32 v48, s3, v9
	v_fmac_f32_e32 v49, s4, v9
	v_fmac_f32_e32 v50, s5, v9
	v_fmac_f32_e32 v51, s6, v9
	v_fmac_f32_e32 v52, s7, v9
	v_fmac_f32_e32 v53, s8, v9
	v_fmac_f32_e32 v54, s9, v9
	v_fmac_f32_e32 v55, s10, v9
	v_fmac_f32_e32 v1, s13, v2
	v_fmac_f32_e32 v56, s13, v3
	v_fmac_f32_e32 v37, s22, v2
	v_fmac_f32_e32 v34, s23, v2
	v_fmac_f32_e32 v35, s24, v2
	v_fmac_f32_e32 v36, s25, v2
	v_fmac_f32_e32 v38, s26, v2
	v_fmac_f32_e32 v39, s27, v2
	v_fmac_f32_e32 v46, s2, v2
	v_fmac_f32_e32 v47, s3, v2
	v_fmac_f32_e32 v48, s4, v2
	v_fmac_f32_e32 v49, s5, v2
	v_fmac_f32_e32 v50, s6, v2
	v_fmac_f32_e32 v51, s7, v2
	v_fmac_f32_e32 v52, s8, v2
	v_fmac_f32_e32 v53, s9, v2
	v_fmac_f32_e32 v54, s10, v2
	v_fmac_f32_e32 v55, s11, v2
	v_fmac_f32_e32 v1, s14, v3
	v_fmac_f32_e32 v56, s14, v4
	v_fmac_f32_e32 v37, s23, v3
	v_fmac_f32_e32 v34, s24, v3
	v_fmac_f32_e32 v35, s25, v3
	v_fmac_f32_e32 v36, s26, v3
	v_fmac_f32_e32 v38, s27, v3
	v_fmac_f32_e32 v39, s28, v3
	v_fmac_f32_e32 v45, s2, v3
	v_fmac_f32_e32 v46, s3, v3
	v_fmac_f32_e32 v47, s4, v3
	v_fmac_f32_e32 v48, s5, v3
	v_fmac_f32_e32 v49, s6, v3
	v_fmac_f32_e32 v50, s7, v3
	v_fmac_f32_e32 v51, s8, v3
	v_fmac_f32_e32 v52, s9, v3
	v_fmac_f32_e32 v53, s10, v3
	v_fmac_f32_e32 v54, s11, v3
	v_fmac_f32_e32 v55, s12, v3
	v_fmac_f32_e32 v1, s15, v4
	v_fmac_f32_e32 v56, s15, v5
	v_lshrrev_b32_e32 v2, 5, v0
	v_fmac_f32_e32 v37, s24, v4
	v_fmac_f32_e32 v34, s25, v4
	v_fmac_f32_e32 v35, s26, v4
	v_fmac_f32_e32 v36, s27, v4
	v_fmac_f32_e32 v38, s28, v4
	v_fmac_f32_e32 v39, s29, v4
	v_fmac_f32_e32 v44, s2, v4
	v_fmac_f32_e32 v45, s3, v4
	v_fmac_f32_e32 v46, s4, v4
	v_fmac_f32_e32 v47, s5, v4
	v_fmac_f32_e32 v48, s6, v4
	v_fmac_f32_e32 v49, s7, v4
	v_fmac_f32_e32 v50, s8, v4
	v_fmac_f32_e32 v51, s9, v4
	v_fmac_f32_e32 v52, s10, v4
	v_fmac_f32_e32 v53, s11, v4
	v_fmac_f32_e32 v54, s12, v4
	v_fmac_f32_e32 v55, s13, v4
	s_waitcnt lgkmcnt(0)
	v_fmac_f32_e32 v1, s0, v5
	v_fmac_f32_e32 v56, s0, v57
	v_lshl_or_b32 v4, s33, 3, v2
	v_mov_b32_e32 v2, s56
	v_mov_b32_e32 v3, 0
	s_movk_i32 s0, 0x240
	v_fmac_f32_e32 v37, s25, v5
	v_fmac_f32_e32 v34, s26, v5
	v_fmac_f32_e32 v35, s27, v5
	v_fmac_f32_e32 v36, s28, v5
	v_fmac_f32_e32 v38, s29, v5
	v_fmac_f32_e32 v39, s30, v5
	v_fmac_f32_e32 v43, s2, v5
	v_fmac_f32_e32 v44, s3, v5
	v_fmac_f32_e32 v45, s4, v5
	v_fmac_f32_e32 v46, s5, v5
	v_fmac_f32_e32 v47, s6, v5
	v_fmac_f32_e32 v48, s7, v5
	v_fmac_f32_e32 v49, s8, v5
	v_fmac_f32_e32 v50, s9, v5
	v_fmac_f32_e32 v51, s10, v5
	v_fmac_f32_e32 v52, s11, v5
	v_fmac_f32_e32 v53, s12, v5
	v_fmac_f32_e32 v54, s13, v5
	v_fmac_f32_e32 v55, s14, v5
	v_fmac_f32_e32 v1, s1, v57
	v_mad_u64_u32 v[4:5], s[0:1], v4, s0, v[2:3]
	v_fmac_f32_e32 v37, s26, v57
	v_fmac_f32_e32 v34, s27, v57
	v_fmac_f32_e32 v35, s28, v57
	v_fmac_f32_e32 v36, s29, v57
	v_fmac_f32_e32 v38, s30, v57
	v_fmac_f32_e32 v39, s31, v57
	v_fmac_f32_e32 v42, s2, v57
	v_fmac_f32_e32 v43, s3, v57
	v_fmac_f32_e32 v44, s4, v57
	v_fmac_f32_e32 v45, s5, v57
	v_fmac_f32_e32 v46, s6, v57
	v_fmac_f32_e32 v47, s7, v57
	v_fmac_f32_e32 v48, s8, v57
	v_fmac_f32_e32 v49, s9, v57
	v_fmac_f32_e32 v50, s10, v57
	v_fmac_f32_e32 v51, s11, v57
	v_fmac_f32_e32 v52, s12, v57
	v_fmac_f32_e32 v53, s13, v57
	v_fmac_f32_e32 v54, s14, v57
	v_fmac_f32_e32 v55, s15, v57
	v_lshlrev_b64 v[4:5], 6, v[4:5]
	v_lshl_add_u64 v[4:5], s[58:59], 0, v[4:5]
	s_mov_b32 s0, 0x42800000
	v_lshrrev_b32_e32 v2, 5, v0
	v_and_b32_e32 v3, 31, v0
	v_mul_u32_u24_e32 v2, 0x600, v2
	v_lshl_add_u32 v2, v3, 1, v2
	v_max_f32_e32 v3, 0, v37
	v_fma_mixlo_f16 v3, v3, s0, 0
	ds_write_b16 v2, v3
	v_max_f32_e32 v58, 0, v34
	v_fma_mixlo_f16 v58, v58, s0, 0
	ds_write_b16 v2, v58 offset:64
	v_max_f32_e32 v3, 0, v35
	v_fma_mixlo_f16 v3, v3, s0, 0
	ds_write_b16 v2, v3 offset:128
	v_max_f32_e32 v58, 0, v36
	v_fma_mixlo_f16 v58, v58, s0, 0
	ds_write_b16 v2, v58 offset:192
	v_max_f32_e32 v3, 0, v38
	v_fma_mixlo_f16 v3, v3, s0, 0
	ds_write_b16 v2, v3 offset:256
	v_max_f32_e32 v58, 0, v39
	v_fma_mixlo_f16 v58, v58, s0, 0
	ds_write_b16 v2, v58 offset:320
	v_max_f32_e32 v3, 0, v40
	v_fma_mixlo_f16 v3, v3, s0, 0
	ds_write_b16 v2, v3 offset:384
	v_max_f32_e32 v58, 0, v41
	v_fma_mixlo_f16 v58, v58, s0, 0
	ds_write_b16 v2, v58 offset:448
	v_max_f32_e32 v3, 0, v42
	v_fma_mixlo_f16 v3, v3, s0, 0
	ds_write_b16 v2, v3 offset:512
	v_max_f32_e32 v58, 0, v43
	v_fma_mixlo_f16 v58, v58, s0, 0
	ds_write_b16 v2, v58 offset:576
	v_max_f32_e32 v3, 0, v44
	v_fma_mixlo_f16 v3, v3, s0, 0
	ds_write_b16 v2, v3 offset:640
	v_max_f32_e32 v58, 0, v45
	v_fma_mixlo_f16 v58, v58, s0, 0
	ds_write_b16 v2, v58 offset:704
	v_max_f32_e32 v3, 0, v46
	v_fma_mixlo_f16 v3, v3, s0, 0
	ds_write_b16 v2, v3 offset:768
	v_max_f32_e32 v58, 0, v47
	v_fma_mixlo_f16 v58, v58, s0, 0
	ds_write_b16 v2, v58 offset:832
	v_max_f32_e32 v3, 0, v48
	v_fma_mixlo_f16 v3, v3, s0, 0
	ds_write_b16 v2, v3 offset:896
	v_max_f32_e32 v58, 0, v49
	v_fma_mixlo_f16 v58, v58, s0, 0
	ds_write_b16 v2, v58 offset:960
	v_max_f32_e32 v3, 0, v50
	v_fma_mixlo_f16 v3, v3, s0, 0
	ds_write_b16 v2, v3 offset:1024
	v_max_f32_e32 v58, 0, v51
	v_fma_mixlo_f16 v58, v58, s0, 0
	ds_write_b16 v2, v58 offset:1088
	v_max_f32_e32 v3, 0, v52
	v_fma_mixlo_f16 v3, v3, s0, 0
	ds_write_b16 v2, v3 offset:1152
	v_max_f32_e32 v58, 0, v53
	v_fma_mixlo_f16 v58, v58, s0, 0
	ds_write_b16 v2, v58 offset:1216
	v_max_f32_e32 v3, 0, v54
	v_fma_mixlo_f16 v3, v3, s0, 0
	ds_write_b16 v2, v3 offset:1280
	v_max_f32_e32 v58, 0, v55
	v_fma_mixlo_f16 v58, v58, s0, 0
	ds_write_b16 v2, v58 offset:1344
	v_max_f32_e32 v3, 0, v56
	v_fma_mixlo_f16 v3, v3, s0, 0
	ds_write_b16 v2, v3 offset:1408
	v_max_f32_e32 v58, 0, v1
	v_fma_mixlo_f16 v58, v58, s0, 0
	ds_write_b16 v2, v58 offset:1472
	v_and_b32_e32 v6, 63, v0
	v_lshrrev_b32_e32 v7, 6, v0
	v_mul_u32_u24_e32 v7, 0xc00, v7
	v_lshl_add_u32 v7, v6, 4, v7
	ds_read_b128 v[10:13], v7
	ds_read_b128 v[14:17], v7 offset:1024
	ds_read_b128 v[18:21], v7 offset:2048
	v_readfirstlane_b32 s62, v4
	v_readfirstlane_b32 s63, v5
	v_cmp_gt_u32_e64 s[60:61], 32, v6
	v_lshlrev_b32_e32 v22, 4, v6
	v_add_u32_e32 v23, 0x400, v22
	v_add_u32_e32 v24, 0x8e00, v22
	v_add_u32_e32 v25, 0x9200, v22
	v_cndmask_b32_e64 v23, v24, v23, s[60:61]
	s_waitcnt lgkmcnt(0)
	global_store_dwordx4 v22, v[10:13], s[62:63]
	global_store_dwordx4 v23, v[14:17], s[62:63]
	global_store_dwordx4 v25, v[18:21], s[62:63]
	s_endpgm

	.amdhsa_kernel _Z12conv1_kernelPKfS0_S0_PDF16_
		.amdhsa_group_segment_fixed_size 12288
		.amdhsa_private_segment_fixed_size 0
		.amdhsa_kernarg_size 32
		.amdhsa_user_sgpr_count 2
		.amdhsa_user_sgpr_dispatch_ptr 0
		.amdhsa_user_sgpr_queue_ptr 0
		.amdhsa_user_sgpr_kernarg_segment_ptr 1
		.amdhsa_user_sgpr_dispatch_id 0
		.amdhsa_user_sgpr_kernarg_preload_length 0
		.amdhsa_user_sgpr_kernarg_preload_offset 0
		.amdhsa_user_sgpr_private_segment_size 0
		.amdhsa_uses_dynamic_stack 0
		.amdhsa_enable_private_segment 0
		.amdhsa_system_sgpr_workgroup_id_x 1
		.amdhsa_system_sgpr_workgroup_id_y 0
		.amdhsa_system_sgpr_workgroup_id_z 0
		.amdhsa_system_sgpr_workgroup_info 0
		.amdhsa_system_vgpr_workitem_id 0
		.amdhsa_next_free_vgpr 59
		.amdhsa_next_free_sgpr 64
		.amdhsa_accum_offset 60
		.amdhsa_reserve_vcc 0
		.amdhsa_float_round_mode_32 0
		.amdhsa_float_round_mode_16_64 0
		.amdhsa_float_denorm_mode_32 3
		.amdhsa_float_denorm_mode_16_64 3
		.amdhsa_dx10_clamp 1
		.amdhsa_ieee_mode 1
		.amdhsa_fp16_overflow 0
		.amdhsa_tg_split 0
		.amdhsa_exception_fp_ieee_invalid_op 0
		.amdhsa_exception_fp_denorm_src 0
		.amdhsa_exception_fp_ieee_div_zero 0
		.amdhsa_exception_fp_ieee_overflow 0
		.amdhsa_exception_fp_ieee_underflow 0
		.amdhsa_exception_fp_ieee_inexact 0
		.amdhsa_exception_int_div_zero 0
	.end_amdhsa_kernel

amdhsa.kernels:
  - .agpr_count:     16
    .args:
      - .address_space:  global
        .offset:         0
        .size:           8
        .value_kind:     global_buffer
      - .address_space:  global
        .offset:         8
        .size:           8
        .value_kind:     global_buffer
      - .address_space:  global
        .offset:         16
        .size:           8
        .value_kind:     global_buffer
      - .address_space:  global
        .offset:         24
        .size:           8
        .value_kind:     global_buffer
      - .address_space:  global
        .offset:         32
        .size:           8
        .value_kind:     global_buffer
      - .address_space:  global
        .offset:         40
        .size:           8
        .value_kind:     global_buffer
      - .address_space:  global
        .offset:         48
        .size:           8
        .value_kind:     global_buffer
      - .address_space:  global
        .offset:         56
        .size:           8
        .value_kind:     global_buffer
      - .address_space:  global
        .offset:         64
        .size:           8
        .value_kind:     global_buffer
      - .address_space:  global
        .offset:         72
        .size:           8
        .value_kind:     global_buffer
      - .address_space:  global
        .offset:         80
        .size:           8
        .value_kind:     global_buffer
      - .address_space:  global
        .offset:         88
        .size:           8
        .value_kind:     global_buffer
      - .address_space:  global
        .offset:         96
        .size:           8
        .value_kind:     global_buffer
      - .address_space:  global
        .offset:         104
        .size:           8
        .value_kind:     global_buffer
      - .address_space:  global
        .offset:         112
        .size:           8
        .value_kind:     global_buffer
      - .address_space:  global
        .offset:         120
        .size:           8
        .value_kind:     global_buffer
      - .address_space:  global
        .offset:         128
        .size:           8
        .value_kind:     global_buffer
      - .address_space:  global
        .offset:         136
        .size:           8
        .value_kind:     global_buffer
      - .address_space:  global
        .offset:         144
        .size:           8
        .value_kind:     global_buffer
      - .address_space:  global
        .offset:         152
        .size:           8
        .value_kind:     global_buffer
    .group_segment_fixed_size: 0
    .kernarg_segment_align: 8
    .kernarg_segment_size: 160
    .language:       OpenCL C
    .language_version:
      - 2
      - 0
    .max_flat_workgroup_size: 256
    .name:           _Z11lstm_kernelPKDF16_PKDv8_DF16_S3_S3_PKfS5_S5_S5_PDF16_S6_PfS5_PS1_PK15HIP_vector_typeIfLj4EES5_S5_S7_S5_S5_S5_
    .private_segment_fixed_size: 0
    .sgpr_count:     70
    .sgpr_spill_count: 0
    .symbol:         _Z11lstm_kernelPKDF16_PKDv8_DF16_S3_S3_PKfS5_S5_S5_PDF16_S6_PfS5_PS1_PK15HIP_vector_typeIfLj4EES5_S5_S7_S5_S5_S5_.kd
    .uniform_work_group_size: 1
    .uses_dynamic_stack: false
    .vgpr_count:     228
    .vgpr_spill_count: 0
    .wavefront_size: 64
  - .agpr_count:     0
    .args:
      - .actual_access:  read_only
        .address_space:  global
        .offset:         0
        .size:           8
        .value_kind:     global_buffer
      - .actual_access:  read_only
        .address_space:  global
        .offset:         8
        .size:           8
        .value_kind:     global_buffer
      - .actual_access:  read_only
        .address_space:  global
        .offset:         16
        .size:           8
        .value_kind:     global_buffer
      - .actual_access:  write_only
        .address_space:  global
        .offset:         24
        .size:           8
        .value_kind:     global_buffer
    .group_segment_fixed_size: 12288
    .kernarg_segment_align: 8
    .kernarg_segment_size: 32
    .language:       OpenCL C
    .language_version:
      - 2
      - 0
    .max_flat_workgroup_size: 256
    .name:           _Z12conv1_kernelPKfS0_S0_PDF16_
    .private_segment_fixed_size: 0
    .sgpr_count:     70
    .sgpr_spill_count: 0
    .symbol:         _Z12conv1_kernelPKfS0_S0_PDF16_.kd
    .uniform_work_group_size: 1
    .uses_dynamic_stack: false
    .vgpr_count:     59
    .vgpr_spill_count: 0
    .wavefront_size: 64
  - .agpr_count:     0
    .args:
      - .address_space:  global
        .offset:         0
        .size:           8
        .value_kind:     global_buffer
      - .address_space:  global
        .offset:         8
        .size:           8
        .value_kind:     global_buffer
      - .address_space:  global
        .offset:         16
        .size:           8
        .value_kind:     global_buffer
      - .address_space:  global
        .offset:         24
        .size:           8
        .value_kind:     global_buffer
      - .address_space:  global
        .offset:         32
        .size:           8
        .value_kind:     global_buffer
      - .address_space:  global
        .offset:         40
        .size:           8
        .value_kind:     global_buffer
      - .address_space:  global
        .offset:         48
        .size:           8
        .value_kind:     global_buffer
      - .address_space:  global
        .offset:         56
        .size:           8
        .value_kind:     global_buffer
      - .address_space:  global
        .offset:         64
        .size:           8
        .value_kind:     global_buffer
      - .address_space:  global
        .offset:         72
        .size:           8
        .value_kind:     global_buffer
      - .address_space:  global
        .offset:         80
        .size:           8
        .value_kind:     global_buffer
    .group_segment_fixed_size: 0
    .kernarg_segment_align: 8
    .kernarg_segment_size: 88
    .language:       OpenCL C
    .language_version:
      - 2
      - 0
    .max_flat_workgroup_size: 256
    .name:           _Z11prep_kernelPKfS0_S0_S0_PDv8_DF16_S2_S2_PKiS0_S2_PDv4_j
    .private_segment_fixed_size: 0
    .sgpr_count:     34
    .sgpr_spill_count: 0
    .symbol:         _Z11prep_kernelPKfS0_S0_S0_PDv8_DF16_S2_S2_PKiS0_S2_PDv4_j.kd
    .uniform_work_group_size: 1
    .uses_dynamic_stack: false
    .vgpr_count:     17
    .vgpr_spill_count: 0
    .wavefront_size: 64
  - .agpr_count:     104
    .args:
      - .address_space:  global
        .offset:         0
        .size:           8
        .value_kind:     global_buffer
      - .address_space:  global
        .offset:         8
        .size:           8
        .value_kind:     global_buffer
      - .address_space:  global
        .offset:         16
        .size:           8
        .value_kind:     global_buffer
      - .address_space:  global
        .offset:         24
        .size:           8
        .value_kind:     global_buffer
      - .address_space:  global
        .offset:         32
        .size:           8
        .value_kind:     global_buffer
    .group_segment_fixed_size: 129152
    .kernarg_segment_align: 8
    .kernarg_segment_size: 40
    .language:       OpenCL C
    .language_version:
      - 2
      - 0
    .max_flat_workgroup_size: 256
    .name:           _Z13pconv2_kernelPKDF16_PKDv8_DF16_PKfPfS6_
    .private_segment_fixed_size: 0
    .sgpr_count:     30
    .sgpr_spill_count: 0
    .symbol:         _Z13pconv2_kernelPKDF16_PKDv8_DF16_PKfPfS6_.kd
    .uniform_work_group_size: 1
    .uses_dynamic_stack: false
    .vgpr_count:     324
    .vgpr_spill_count: 0
    .wavefront_size: 64
  - .agpr_count:     40
    .args:
      - .address_space:  global
        .offset:         0
        .size:           8
        .value_kind:     global_buffer
      - .address_space:  global
        .offset:         8
        .size:           8
        .value_kind:     global_buffer
      - .address_space:  global
        .offset:         16
        .size:           8
        .value_kind:     global_buffer
      - .address_space:  global
        .offset:         24
        .size:           8
        .value_kind:     global_buffer
    .group_segment_fixed_size: 41472
    .kernarg_segment_align: 8
    .kernarg_segment_size: 32
    .language:       OpenCL C
    .language_version:
      - 2
      - 0
    .max_flat_workgroup_size: 256
    .name:           _Z11dcap_kernelPKfS0_S0_Pf
    .private_segment_fixed_size: 0
    .sgpr_count:     25
    .sgpr_spill_count: 0
    .symbol:         _Z11dcap_kernelPKfS0_S0_Pf.kd
    .uniform_work_group_size: 1
    .uses_dynamic_stack: false
    .vgpr_count:     244
    .vgpr_spill_count: 0
    .wavefront_size: 64
  - .agpr_count:     0
    .args:
      - .address_space:  global
        .offset:         0
        .size:           8
        .value_kind:     global_buffer
      - .address_space:  global
        .offset:         8
        .size:           8
        .value_kind:     global_buffer
    .group_segment_fixed_size: 3200
    .kernarg_segment_align: 8
    .kernarg_segment_size: 16
    .language:       OpenCL C
    .language_version:
      - 2
      - 0
    .max_flat_workgroup_size: 640
    .name:           _Z12final_kernelPKfPf
    .private_segment_fixed_size: 0
    .sgpr_count:     16
    .sgpr_spill_count: 0
    .symbol:         _Z12final_kernelPKfPf.kd
    .uniform_work_group_size: 1
    .uses_dynamic_stack: false
    .vgpr_count:     78
    .vgpr_spill_count: 0
    .wavefront_size: 64
